# dense-up and MoE-up int8 GEMMs: per-unit accumulator zeroing removed, first K iteration uses C=0 MFMA variants
# baseline (speedup 1.0000x reference)
; template <bool I8, class AccT> __device__ __forceinline__ void mma1(AccT& c, const bf16x8& a, const bf16x8& b) {
;     if constexpr (I8) c = __builtin_amdgcn_mfma_i32_16x16x64_i8(__builtin_bit_cast(AccT, a), __builtin_bit_cast(AccT, b), c, 0, 0, 0);
;     else c = __builtin_amdgcn_mfma_f32_16x16x32_bf16(a, b, c, 0, 0, 0);
; }
.Lzmu_s0:
	v_mfma_i32_16x16x64_i8 v[126:129], v[136:139], v[174:177], 0
	v_mfma_i32_16x16x64_i8 v[118:121], v[146:149], v[174:177], 0
	v_mfma_i32_16x16x64_i8 v[108:111], v[136:139], v[182:185], 0
	v_mfma_i32_16x16x64_i8 v[100:103], v[146:149], v[182:185], 0
	v_mfma_i32_16x16x64_i8 v[92:95], v[136:139], v[190:193], 0
	v_mfma_i32_16x16x64_i8 v[84:87], v[146:149], v[190:193], 0
	v_mfma_i32_16x16x64_i8 v[76:79], v[136:139], v[198:201], 0
	v_mfma_i32_16x16x64_i8 v[68:71], v[146:149], v[198:201], 0
	v_mfma_i32_16x16x64_i8 v[126:129], v[140:143], v[178:181], v[126:129]
	v_mfma_i32_16x16x64_i8 v[118:121], v[150:153], v[178:181], v[118:121]
	v_mfma_i32_16x16x64_i8 v[108:111], v[140:143], v[186:189], v[108:111]
	v_mfma_i32_16x16x64_i8 v[100:103], v[150:153], v[186:189], v[100:103]
	v_mfma_i32_16x16x64_i8 v[92:95], v[140:143], v[194:197], v[92:95]
	v_mfma_i32_16x16x64_i8 v[84:87], v[150:153], v[194:197], v[84:87]
	v_mfma_i32_16x16x64_i8 v[76:79], v[140:143], v[202:205], v[76:79]
	v_mfma_i32_16x16x64_i8 v[68:71], v[150:153], v[202:205], v[68:71]
	s_setprio 0
	s_setprio 1
	v_mfma_i32_16x16x64_i8 v[122:125], v[154:157], v[174:177], 0
	v_mfma_i32_16x16x64_i8 v[114:117], v[166:169], v[174:177], 0
	v_mfma_i32_16x16x64_i8 v[104:107], v[154:157], v[182:185], 0
	v_mfma_i32_16x16x64_i8 v[96:99], v[166:169], v[182:185], 0
	v_mfma_i32_16x16x64_i8 v[88:91], v[154:157], v[190:193], 0
	v_mfma_i32_16x16x64_i8 v[80:83], v[166:169], v[190:193], 0
	v_mfma_i32_16x16x64_i8 v[72:75], v[154:157], v[198:201], 0
	v_mfma_i32_16x16x64_i8 v[64:67], v[166:169], v[198:201], 0
	v_mfma_i32_16x16x64_i8 v[122:125], v[158:161], v[178:181], v[122:125]
	v_mfma_i32_16x16x64_i8 v[114:117], v[170:173], v[178:181], v[114:117]
	v_mfma_i32_16x16x64_i8 v[104:107], v[158:161], v[186:189], v[104:107]
	v_mfma_i32_16x16x64_i8 v[96:99], v[170:173], v[186:189], v[96:99]
	v_mfma_i32_16x16x64_i8 v[88:91], v[158:161], v[194:197], v[88:91]
	v_mfma_i32_16x16x64_i8 v[80:83], v[170:173], v[194:197], v[80:83]
	v_mfma_i32_16x16x64_i8 v[72:75], v[158:161], v[202:205], v[72:75]
	v_mfma_i32_16x16x64_i8 v[64:67], v[170:173], v[202:205], v[64:67]
	s_setprio 0
	s_branch .Lzmu_r0
.Lzmu_s1:
	v_mfma_i32_16x16x64_i8 v[60:63], v[136:139], v[174:177], 0
	v_mfma_i32_16x16x64_i8 v[52:55], v[146:149], v[174:177], 0
	v_mfma_i32_16x16x64_i8 v[44:47], v[136:139], v[182:185], 0
	v_mfma_i32_16x16x64_i8 v[36:39], v[146:149], v[182:185], 0
	v_mfma_i32_16x16x64_i8 v[28:31], v[136:139], v[190:193], 0
	v_mfma_i32_16x16x64_i8 v[20:23], v[146:149], v[190:193], 0
	v_mfma_i32_16x16x64_i8 v[12:15], v[136:139], v[198:201], 0
	v_mfma_i32_16x16x64_i8 v[4:7], v[146:149], v[198:201], 0
	v_mfma_i32_16x16x64_i8 v[60:63], v[140:143], v[178:181], v[60:63]
	v_mfma_i32_16x16x64_i8 v[52:55], v[150:153], v[178:181], v[52:55]
	v_mfma_i32_16x16x64_i8 v[44:47], v[140:143], v[186:189], v[44:47]
	v_mfma_i32_16x16x64_i8 v[36:39], v[150:153], v[186:189], v[36:39]
	v_mfma_i32_16x16x64_i8 v[28:31], v[140:143], v[194:197], v[28:31]
	v_mfma_i32_16x16x64_i8 v[20:23], v[150:153], v[194:197], v[20:23]
	v_mfma_i32_16x16x64_i8 v[12:15], v[140:143], v[202:205], v[12:15]
	v_mfma_i32_16x16x64_i8 v[4:7], v[150:153], v[202:205], v[4:7]
	s_setprio 0
	s_setprio 1
	v_mfma_i32_16x16x64_i8 v[56:59], v[154:157], v[174:177], 0
	v_mfma_i32_16x16x64_i8 v[48:51], v[166:169], v[174:177], 0
	v_mfma_i32_16x16x64_i8 v[40:43], v[154:157], v[182:185], 0
	v_mfma_i32_16x16x64_i8 v[32:35], v[166:169], v[182:185], 0
	v_mfma_i32_16x16x64_i8 v[24:27], v[154:157], v[190:193], 0
	v_mfma_i32_16x16x64_i8 v[16:19], v[166:169], v[190:193], 0
	v_mfma_i32_16x16x64_i8 v[8:11], v[154:157], v[198:201], 0
	v_mfma_i32_16x16x64_i8 v[0:3], v[166:169], v[198:201], 0
	v_mfma_i32_16x16x64_i8 v[56:59], v[158:161], v[178:181], v[56:59]
	v_mfma_i32_16x16x64_i8 v[48:51], v[170:173], v[178:181], v[48:51]
	v_mfma_i32_16x16x64_i8 v[40:43], v[158:161], v[186:189], v[40:43]
	v_mfma_i32_16x16x64_i8 v[32:35], v[170:173], v[186:189], v[32:35]
	v_mfma_i32_16x16x64_i8 v[24:27], v[158:161], v[194:197], v[24:27]
	v_mfma_i32_16x16x64_i8 v[16:19], v[170:173], v[194:197], v[16:19]
	v_mfma_i32_16x16x64_i8 v[8:11], v[158:161], v[202:205], v[8:11]
	v_mfma_i32_16x16x64_i8 v[0:3], v[170:173], v[202:205], v[0:3]
	s_setprio 0
	s_branch .Lzmu_r1

; #define PG8_STAGE(bufoff, gbase, voff) do { _Pragma("unroll") for (int _i = 0; _i < 2; ++_i) { const char* gb_ = (const char*)(gbase) + _i * rstep; asm volatile("" : "+s"(gb_));   \
;         __builtin_amdgcn_global_load_lds((const unsigned*)(gb_ + (voff)), (LAS unsigned*)(lds + (bufoff) + ldsw + _i * 8192), 16, 0, 0); } } while (0)
; #define PG8_LDA(dst, b, h) do { _Pragma("unroll") for (int m = 0; m < 4; ++m) _Pragma("unroll") for (int k = 0; k < 2; ++k) dst[m][k] = *(const LAS bf16x8*)(lds + PG8_SA(b, h) + aoff + m * 2048 + k * 1024); } while (0)
; #define PG8_WAIT_V(n) asm volatile("s_waitcnt vmcnt(" #n ")" ::: "memory")
; #define PG8_WAIT_L(n) asm volatile("s_waitcnt lgkmcnt(" #n ")" ::: "memory")
; #define PG8_BAR __builtin_amdgcn_s_barrier()
; template <class Epi, class Sched, bool ALIGN_EPI = true, bool SP2 = true, bool I8 = false, bool F8 = false>
; __device__ __forceinline__ void gemm_phase(LAS unsigned char* lds, const int K, const Sched& S, const Epi& E, const int wave) {
;     ...
;         const bool has_next = S.next(ui + 1, nxt);
;         const char* nA = has_next ? nxt.a : cA; const char* nB = has_next ? nxt.b : cB;
;         for (int t = 0; t < nt; t += 2) {
;             const bool last = (t == nt - 2);
;             const char* a1 = cA + (size_t)(t + 1) * kstep;
;             const char* a2 = last ? nA : cA + (size_t)(t + 2) * kstep; const char* b2 = last ? nB : cB + (size_t)(t + 2) * kstep;
;             const char* a3 = a2 + kstep; const char* b3 = b2 + kstep;
;             if constexpr (SP2) {
;             PG8_LDB(B0, 0, 0); PG8_LDB(B1, 0, 1); PG8_SCHED; PG8_LDA(At, 0, 0); PG8_STAGE(PG8_SA(1, 1), a1 + hstep, voffA);
;             PG8_WAIT_V(8); PG8_WAIT_L(0); PG8_BAR; PG8_MMA(0, 0, At, B0); PG8_MMA(0, 1, At, B1); PG8_BAR; PG8_SCHED;
;             PG8_LDA(At, 0, 1); PG8_STAGE(PG8_SB(0, 0), b2, voffB); PG8_STAGE(PG8_SB(0, 1), b2 + hstep, voffB); PG8_STAGE(PG8_SA(0, 0), a2, voffA);
;             PG8_WAIT_V(8); PG8_WAIT_L(0); PG8_BAR; PG8_MMA(1, 0, At, B0); PG8_MMA(1, 1, At, B1); PG8_BAR; PG8_SCHED;
;     ...
;         if (!(Epi::KEEPS && cur.sub < 2)) {
; #pragma unroll
;         for (int a = 0; a < 2; ++a)
; #pragma unroll
;             for (int b = 0; b < 2; ++b)
; #pragma unroll
;                 for (int m = 0; m < 4; ++m)
; #pragma unroll
;                     for (int n = 0; n < 2; ++n) acc[a][b][m][n] = (acc_t){0, 0, 0, 0};
;         }
.LBB0_1539:
	s_add_u32 s11, s24, 0x100
	s_addc_u32 s13, s25, 0
	s_add_u32 s22, s22, 0x30080
	s_addc_u32 s23, s23, 0
	s_mov_b32 s19, -2
.LBB0_1540:
	s_add_u32 s21, s22, 0xfffd0080
	s_addc_u32 s24, s23, -1
	s_cmp_eq_u32 s19, 4
	s_cselect_b32 s25, s15, s24
	s_cselect_b32 s24, s14, s21
	s_cselect_b32 s28, s16, s11
	s_cselect_b32 s29, s17, s13
	s_add_u32 s26, s24, 0x80
	s_addc_u32 s27, s25, 0
	s_add_i32 s21, 0, 0x10000
	v_add_u32_e32 v132, s21, v135
	s_add_i32 s63, 0, 0x14000
	ds_read_b128 v[136:139], v132
	ds_read_b128 v[140:143], v132 offset:1024
	ds_read_b128 v[146:149], v132 offset:2048
	ds_read_b128 v[150:153], v132 offset:3072
	v_add_u32_e32 v132, s63, v135
	ds_read_b128 v[154:157], v132
	ds_read_b128 v[158:161], v132 offset:1024
	ds_read_b128 v[166:169], v132 offset:2048
	ds_read_b128 v[170:173], v132 offset:3072
	s_add_u32 s68, s22, 0xffff0000
	s_addc_u32 s69, s23, -1
	ds_read_b128 v[174:177], v145
	ds_read_b128 v[178:181], v145 offset:1024
	ds_read_b128 v[182:185], v145 offset:2048
	ds_read_b128 v[186:189], v145 offset:3072
	ds_read_b128 v[190:193], v145 offset:4096
	ds_read_b128 v[194:197], v145 offset:5120
	ds_read_b128 v[198:201], v145 offset:6144
	ds_read_b128 v[202:205], v145 offset:7168
	s_add_i32 m0, s58, 0xc000
	v_lshl_add_u64 v[132:133], s[68:69], 0, v[130:131]
	s_mov_b64 s[68:69], s[22:23]
	global_load_lds_dwordx4 v[132:133], off
	s_add_i32 m0, s58, 0xe000
	v_lshl_add_u64 v[132:133], s[68:69], 0, v[130:131]
	global_load_lds_dwordx4 v[132:133], off
	s_waitcnt vmcnt(8)
	s_waitcnt lgkmcnt(0)
	s_barrier
	s_setprio 1
	s_waitcnt lgkmcnt(0)
	s_cmp_eq_u32 s19, -2
	s_cbranch_scc1 .Lzmu_s0
	v_mfma_i32_16x16x64_i8 v[126:129], v[136:139], v[174:177], v[126:129]
	v_mfma_i32_16x16x64_i8 v[118:121], v[146:149], v[174:177], v[118:121]
	v_mfma_i32_16x16x64_i8 v[108:111], v[136:139], v[182:185], v[108:111]
	v_mfma_i32_16x16x64_i8 v[100:103], v[146:149], v[182:185], v[100:103]
	v_mfma_i32_16x16x64_i8 v[92:95], v[136:139], v[190:193], v[92:95]
	v_mfma_i32_16x16x64_i8 v[84:87], v[146:149], v[190:193], v[84:87]
	v_mfma_i32_16x16x64_i8 v[76:79], v[136:139], v[198:201], v[76:79]
	v_mfma_i32_16x16x64_i8 v[68:71], v[146:149], v[198:201], v[68:71]
	v_mfma_i32_16x16x64_i8 v[126:129], v[140:143], v[178:181], v[126:129]
	v_mfma_i32_16x16x64_i8 v[118:121], v[150:153], v[178:181], v[118:121]
	v_mfma_i32_16x16x64_i8 v[108:111], v[140:143], v[186:189], v[108:111]
	v_mfma_i32_16x16x64_i8 v[100:103], v[150:153], v[186:189], v[100:103]
	v_mfma_i32_16x16x64_i8 v[92:95], v[140:143], v[194:197], v[92:95]
	v_mfma_i32_16x16x64_i8 v[84:87], v[150:153], v[194:197], v[84:87]
	v_mfma_i32_16x16x64_i8 v[76:79], v[140:143], v[202:205], v[76:79]
	v_mfma_i32_16x16x64_i8 v[68:71], v[150:153], v[202:205], v[68:71]
	s_setprio 0
	s_setprio 1
	v_mfma_i32_16x16x64_i8 v[122:125], v[154:157], v[174:177], v[122:125]
	v_mfma_i32_16x16x64_i8 v[114:117], v[166:169], v[174:177], v[114:117]
	v_mfma_i32_16x16x64_i8 v[104:107], v[154:157], v[182:185], v[104:107]
	v_mfma_i32_16x16x64_i8 v[96:99], v[166:169], v[182:185], v[96:99]
	v_mfma_i32_16x16x64_i8 v[88:91], v[154:157], v[190:193], v[88:91]
	v_mfma_i32_16x16x64_i8 v[80:83], v[166:169], v[190:193], v[80:83]
	v_mfma_i32_16x16x64_i8 v[72:75], v[154:157], v[198:201], v[72:75]
	v_mfma_i32_16x16x64_i8 v[64:67], v[166:169], v[198:201], v[64:67]
	v_mfma_i32_16x16x64_i8 v[122:125], v[158:161], v[178:181], v[122:125]
	v_mfma_i32_16x16x64_i8 v[114:117], v[170:173], v[178:181], v[114:117]
	v_mfma_i32_16x16x64_i8 v[104:107], v[158:161], v[186:189], v[104:107]
	v_mfma_i32_16x16x64_i8 v[96:99], v[170:173], v[186:189], v[96:99]
	v_mfma_i32_16x16x64_i8 v[88:91], v[158:161], v[194:197], v[88:91]
	v_mfma_i32_16x16x64_i8 v[80:83], v[170:173], v[194:197], v[80:83]
	v_mfma_i32_16x16x64_i8 v[72:75], v[158:161], v[202:205], v[72:75]
	v_mfma_i32_16x16x64_i8 v[64:67], v[170:173], v[202:205], v[64:67]
	s_setprio 0
.Lzmu_r0:
	s_barrier
	s_mov_b64 s[68:69], s[28:29]
	ds_read_b128 v[174:177], v145 offset:16384
	ds_read_b128 v[178:181], v145 offset:17408
	ds_read_b128 v[182:185], v145 offset:18432
	ds_read_b128 v[186:189], v145 offset:19456
	ds_read_b128 v[190:193], v145 offset:20480
	ds_read_b128 v[194:197], v145 offset:21504
	ds_read_b128 v[198:201], v145 offset:22528
	ds_read_b128 v[202:205], v145 offset:23552
	s_add_i32 s21, s21, s89
	v_lshl_add_u64 v[132:133], s[68:69], 0, v[112:113]
	s_add_u32 s68, s28, 0x10000
	s_mov_b32 m0, s21
	s_addc_u32 s69, s29, 0
	global_load_lds_dwordx4 v[132:133], off
	s_add_i32 m0, s21, 0x2000
	v_lshl_add_u64 v[132:133], s[68:69], 0, v[112:113]
	s_add_u32 s68, s28, 0x20000
	s_addc_u32 s69, s29, 0
	global_load_lds_dwordx4 v[132:133], off
	s_add_i32 s21, s63, s89
	v_lshl_add_u64 v[132:133], s[68:69], 0, v[112:113]
	s_add_u32 s68, s28, 0x30000
	s_mov_b32 m0, s21
	s_addc_u32 s69, s29, 0
	global_load_lds_dwordx4 v[132:133], off
	s_add_i32 m0, s21, 0x2000
	v_lshl_add_u64 v[132:133], s[68:69], 0, v[112:113]
	s_mov_b64 s[68:69], s[24:25]
	global_load_lds_dwordx4 v[132:133], off
	s_mov_b32 m0, s58
	v_lshl_add_u64 v[132:133], s[68:69], 0, v[130:131]
	s_add_u32 s68, s24, 0x10000
	s_addc_u32 s69, s25, 0
	global_load_lds_dwordx4 v[132:133], off
	s_mov_b32 m0, s73
	v_lshl_add_u64 v[132:133], s[68:69], 0, v[130:131]
	global_load_lds_dwordx4 v[132:133], off
	s_waitcnt vmcnt(8)
	s_waitcnt lgkmcnt(0)
	s_barrier
	s_setprio 1
	s_waitcnt lgkmcnt(0)
	s_cmp_eq_u32 s19, -2
	s_cbranch_scc1 .Lzmu_s1
; #define PG8_STAGE(bufoff, gbase, voff) do { _Pragma("unroll") for (int _i = 0; _i < 2; ++_i) { const char* gb_ = (const char*)(gbase) + _i * rstep; asm volatile("" : "+s"(gb_));   \
;         __builtin_amdgcn_global_load_lds((const unsigned*)(gb_ + (voff)), (LAS unsigned*)(lds + (bufoff) + ldsw + _i * 8192), 16, 0, 0); } } while (0)
; #define PG8_LDA(dst, b, h) do { _Pragma("unroll") for (int m = 0; m < 4; ++m) _Pragma("unroll") for (int k = 0; k < 2; ++k) dst[m][k] = *(const LAS bf16x8*)(lds + PG8_SA(b, h) + aoff + m * 2048 + k * 1024); } while (0)
; #define PG8_LDB(dst, b, h) do { _Pragma("unroll") for (int n = 0; n < 2; ++n) _Pragma("unroll") for (int k = 0; k < 2; ++k) dst[n][k] = *(const LAS bf16x8*)(lds + PG8_SB(b, h) + boff + n * 2048 + k * 1024); } while (0)
; #define PG8_WAIT_V(n) asm volatile("s_waitcnt vmcnt(" #n ")" ::: "memory")
; #define PG8_WAIT_L(n) asm volatile("s_waitcnt lgkmcnt(" #n ")" ::: "memory")
; #define PG8_BAR __builtin_amdgcn_s_barrier()
; #define PG8_SCHED __builtin_amdgcn_sched_barrier(0)
; template <class Epi, class Sched, bool ALIGN_EPI = true, bool SP2 = true, bool I8 = false, bool F8 = false>
; __device__ __forceinline__ void gemm_phase(LAS unsigned char* lds, const int K, const Sched& S, const Epi& E, const int wave) {
;     ...
;             PG8_WAIT_V(8); PG8_WAIT_L(0); PG8_BAR; PG8_MMA(1, 0, At, B0); PG8_MMA(1, 1, At, B1); PG8_BAR; PG8_SCHED;
;             PG8_LDB(B0, 1, 0); PG8_LDB(B1, 1, 1); PG8_SCHED; PG8_LDA(At, 1, 0); PG8_STAGE(PG8_SA(0, 1), a2 + hstep, voffA);
;             PG8_WAIT_V(8); PG8_WAIT_L(0); PG8_BAR; PG8_MMA(0, 0, At, B0); PG8_MMA(0, 1, At, B1); PG8_BAR; PG8_SCHED;
	v_mfma_i32_16x16x64_i8 v[60:63], v[136:139], v[174:177], v[60:63]
	v_mfma_i32_16x16x64_i8 v[52:55], v[146:149], v[174:177], v[52:55]
	v_mfma_i32_16x16x64_i8 v[44:47], v[136:139], v[182:185], v[44:47]
	v_mfma_i32_16x16x64_i8 v[36:39], v[146:149], v[182:185], v[36:39]
	v_mfma_i32_16x16x64_i8 v[28:31], v[136:139], v[190:193], v[28:31]
	v_mfma_i32_16x16x64_i8 v[20:23], v[146:149], v[190:193], v[20:23]
	v_mfma_i32_16x16x64_i8 v[12:15], v[136:139], v[198:201], v[12:15]
	v_mfma_i32_16x16x64_i8 v[4:7], v[146:149], v[198:201], v[4:7]
	v_mfma_i32_16x16x64_i8 v[60:63], v[140:143], v[178:181], v[60:63]
	v_mfma_i32_16x16x64_i8 v[52:55], v[150:153], v[178:181], v[52:55]
	v_mfma_i32_16x16x64_i8 v[44:47], v[140:143], v[186:189], v[44:47]
	v_mfma_i32_16x16x64_i8 v[36:39], v[150:153], v[186:189], v[36:39]
	v_mfma_i32_16x16x64_i8 v[28:31], v[140:143], v[194:197], v[28:31]
	v_mfma_i32_16x16x64_i8 v[20:23], v[150:153], v[194:197], v[20:23]
	v_mfma_i32_16x16x64_i8 v[12:15], v[140:143], v[202:205], v[12:15]
	v_mfma_i32_16x16x64_i8 v[4:7], v[150:153], v[202:205], v[4:7]
	s_setprio 0
	s_setprio 1
	v_mfma_i32_16x16x64_i8 v[56:59], v[154:157], v[174:177], v[56:59]
	v_mfma_i32_16x16x64_i8 v[48:51], v[166:169], v[174:177], v[48:51]
	v_mfma_i32_16x16x64_i8 v[40:43], v[154:157], v[182:185], v[40:43]
	v_mfma_i32_16x16x64_i8 v[32:35], v[166:169], v[182:185], v[32:35]
	v_mfma_i32_16x16x64_i8 v[24:27], v[154:157], v[190:193], v[24:27]
	v_mfma_i32_16x16x64_i8 v[16:19], v[166:169], v[190:193], v[16:19]
	v_mfma_i32_16x16x64_i8 v[8:11], v[154:157], v[198:201], v[8:11]
	v_mfma_i32_16x16x64_i8 v[0:3], v[166:169], v[198:201], v[0:3]
	v_mfma_i32_16x16x64_i8 v[56:59], v[158:161], v[178:181], v[56:59]
	v_mfma_i32_16x16x64_i8 v[48:51], v[170:173], v[178:181], v[48:51]
	v_mfma_i32_16x16x64_i8 v[40:43], v[158:161], v[186:189], v[40:43]
	v_mfma_i32_16x16x64_i8 v[32:35], v[170:173], v[186:189], v[32:35]
	v_mfma_i32_16x16x64_i8 v[24:27], v[158:161], v[194:197], v[24:27]
	v_mfma_i32_16x16x64_i8 v[16:19], v[170:173], v[194:197], v[16:19]
	v_mfma_i32_16x16x64_i8 v[8:11], v[158:161], v[202:205], v[8:11]
	v_mfma_i32_16x16x64_i8 v[0:3], v[170:173], v[202:205], v[0:3]
	s_setprio 0
.Lzmu_r1:
	s_barrier
	s_add_i32 s21, 0, 0x18000
	v_add_u32_e32 v132, s21, v135
	s_add_i32 s63, 0, 0x1c000
	ds_read_b128 v[136:139], v132
	ds_read_b128 v[140:143], v132 offset:1024
	ds_read_b128 v[146:149], v132 offset:2048
	ds_read_b128 v[150:153], v132 offset:3072
	v_add_u32_e32 v132, s63, v135
	ds_read_b128 v[154:157], v132
	ds_read_b128 v[158:161], v132 offset:1024
	ds_read_b128 v[166:169], v132 offset:2048
	ds_read_b128 v[170:173], v132 offset:3072
	s_add_u32 s68, s24, 0x20000
	s_addc_u32 s69, s25, 0
	ds_read_b128 v[174:177], v145 offset:32768
	ds_read_b128 v[178:181], v145 offset:33792
	ds_read_b128 v[182:185], v145 offset:34816
	ds_read_b128 v[186:189], v145 offset:35840
	ds_read_b128 v[190:193], v145 offset:36864
	ds_read_b128 v[194:197], v145 offset:37888
	ds_read_b128 v[198:201], v145 offset:38912
	ds_read_b128 v[202:205], v145 offset:39936
	s_mov_b32 m0, s40
	v_lshl_add_u64 v[132:133], s[68:69], 0, v[130:131]
	s_add_u32 s68, s24, 0x30000
	s_addc_u32 s69, s25, 0
	global_load_lds_dwordx4 v[132:133], off
	s_mov_b32 m0, s41
	v_lshl_add_u64 v[132:133], s[68:69], 0, v[130:131]
	global_load_lds_dwordx4 v[132:133], off
	s_waitcnt vmcnt(8)
	s_waitcnt lgkmcnt(0)
	s_barrier
	s_setprio 1
	s_waitcnt lgkmcnt(0)
	v_mfma_i32_16x16x64_i8 v[126:129], v[136:139], v[174:177], v[126:129]
	v_mfma_i32_16x16x64_i8 v[118:121], v[146:149], v[174:177], v[118:121]
	v_mfma_i32_16x16x64_i8 v[108:111], v[136:139], v[182:185], v[108:111]
	v_mfma_i32_16x16x64_i8 v[100:103], v[146:149], v[182:185], v[100:103]
	v_mfma_i32_16x16x64_i8 v[92:95], v[136:139], v[190:193], v[92:95]
	v_mfma_i32_16x16x64_i8 v[84:87], v[146:149], v[190:193], v[84:87]
	v_mfma_i32_16x16x64_i8 v[76:79], v[136:139], v[198:201], v[76:79]
	v_mfma_i32_16x16x64_i8 v[68:71], v[146:149], v[198:201], v[68:71]
	v_mfma_i32_16x16x64_i8 v[126:129], v[140:143], v[178:181], v[126:129]
	v_mfma_i32_16x16x64_i8 v[118:121], v[150:153], v[178:181], v[118:121]
	v_mfma_i32_16x16x64_i8 v[108:111], v[140:143], v[186:189], v[108:111]
	v_mfma_i32_16x16x64_i8 v[100:103], v[150:153], v[186:189], v[100:103]
	v_mfma_i32_16x16x64_i8 v[92:95], v[140:143], v[194:197], v[92:95]
	v_mfma_i32_16x16x64_i8 v[84:87], v[150:153], v[194:197], v[84:87]
	v_mfma_i32_16x16x64_i8 v[76:79], v[140:143], v[202:205], v[76:79]
	v_mfma_i32_16x16x64_i8 v[68:71], v[150:153], v[202:205], v[68:71]
	s_setprio 0
	s_setprio 1
	v_mfma_i32_16x16x64_i8 v[122:125], v[154:157], v[174:177], v[122:125]
	v_mfma_i32_16x16x64_i8 v[114:117], v[166:169], v[174:177], v[114:117]
	v_mfma_i32_16x16x64_i8 v[104:107], v[154:157], v[182:185], v[104:107]
	v_mfma_i32_16x16x64_i8 v[96:99], v[166:169], v[182:185], v[96:99]
	v_mfma_i32_16x16x64_i8 v[88:91], v[154:157], v[190:193], v[88:91]
	v_mfma_i32_16x16x64_i8 v[80:83], v[166:169], v[190:193], v[80:83]
	v_mfma_i32_16x16x64_i8 v[72:75], v[154:157], v[198:201], v[72:75]
	v_mfma_i32_16x16x64_i8 v[64:67], v[166:169], v[198:201], v[64:67]
	v_mfma_i32_16x16x64_i8 v[122:125], v[158:161], v[178:181], v[122:125]
	v_mfma_i32_16x16x64_i8 v[114:117], v[170:173], v[178:181], v[114:117]
	v_mfma_i32_16x16x64_i8 v[104:107], v[158:161], v[186:189], v[104:107]
	v_mfma_i32_16x16x64_i8 v[96:99], v[170:173], v[186:189], v[96:99]
	v_mfma_i32_16x16x64_i8 v[88:91], v[158:161], v[194:197], v[88:91]
	v_mfma_i32_16x16x64_i8 v[80:83], v[170:173], v[194:197], v[80:83]
	v_mfma_i32_16x16x64_i8 v[72:75], v[158:161], v[202:205], v[72:75]
	v_mfma_i32_16x16x64_i8 v[64:67], v[170:173], v[202:205], v[64:67]
	s_setprio 0
	s_barrier
; #define PG8_STAGE(bufoff, gbase, voff) do { _Pragma("unroll") for (int _i = 0; _i < 2; ++_i) { const char* gb_ = (const char*)(gbase) + _i * rstep; asm volatile("" : "+s"(gb_));   \
;         __builtin_amdgcn_global_load_lds((const unsigned*)(gb_ + (voff)), (LAS unsigned*)(lds + (bufoff) + ldsw + _i * 8192), 16, 0, 0); } } while (0)
; #define PG8_LDA(dst, b, h) do { _Pragma("unroll") for (int m = 0; m < 4; ++m) _Pragma("unroll") for (int k = 0; k < 2; ++k) dst[m][k] = *(const LAS bf16x8*)(lds + PG8_SA(b, h) + aoff + m * 2048 + k * 1024); } while (0)
; #define PG8_WAIT_V(n) asm volatile("s_waitcnt vmcnt(" #n ")" ::: "memory")
; #define PG8_WAIT_L(n) asm volatile("s_waitcnt lgkmcnt(" #n ")" ::: "memory")
; #define PG8_BAR __builtin_amdgcn_s_barrier()
; #define PG8_SCHED __builtin_amdgcn_sched_barrier(0)
; template <class Epi, class Sched, bool ALIGN_EPI = true, bool SP2 = true, bool I8 = false, bool F8 = false>
; __device__ __forceinline__ void gemm_phase(LAS unsigned char* lds, const int K, const Sched& S, const Epi& E, const int wave) {
;     ...
;         for (int t = 0; t < nt; t += 2) {
;             const bool last = (t == nt - 2);
;     ...
;             PG8_LDA(At, 1, 1); PG8_STAGE(PG8_SB(1, 0), b3, voffB); PG8_STAGE(PG8_SB(1, 1), b3 + hstep, voffB); PG8_STAGE(PG8_SA(1, 0), a3, voffA);
;             PG8_WAIT_V(8); PG8_WAIT_L(0); PG8_BAR; PG8_MMA(1, 0, At, B0); PG8_MMA(1, 1, At, B1); PG8_BAR; PG8_SCHED;
	s_add_u32 s68, s28, 0x80
	s_addc_u32 s69, s29, 0
	ds_read_b128 v[174:177], v145 offset:49152
	ds_read_b128 v[178:181], v145 offset:50176
	ds_read_b128 v[182:185], v145 offset:51200
	ds_read_b128 v[186:189], v145 offset:52224
	ds_read_b128 v[190:193], v145 offset:53248
	ds_read_b128 v[194:197], v145 offset:54272
	ds_read_b128 v[198:201], v145 offset:55296
	ds_read_b128 v[202:205], v145 offset:56320
	s_add_i32 s21, s21, s89
	v_lshl_add_u64 v[132:133], s[68:69], 0, v[112:113]
	s_add_u32 s68, s28, 0x10080
	s_mov_b32 m0, s21
	s_addc_u32 s69, s29, 0
	global_load_lds_dwordx4 v[132:133], off
	s_add_i32 m0, s21, 0x2000
	v_lshl_add_u64 v[132:133], s[68:69], 0, v[112:113]
	s_add_u32 s68, s28, 0x20080
	s_addc_u32 s69, s29, 0
	s_add_i32 s21, s63, s89
	global_load_lds_dwordx4 v[132:133], off
	s_mov_b32 m0, s21
	v_lshl_add_u64 v[132:133], s[68:69], 0, v[112:113]
	s_add_u32 s28, s28, 0x30080
	global_load_lds_dwordx4 v[132:133], off
	s_addc_u32 s29, s29, 0
	s_add_i32 m0, s21, 0x2000
	s_add_u32 s24, s24, 0x10080
	v_lshl_add_u64 v[132:133], s[28:29], 0, v[112:113]
	global_load_lds_dwordx4 v[132:133], off
	s_mov_b32 m0, s59
	v_lshl_add_u64 v[132:133], s[26:27], 0, v[130:131]
	s_addc_u32 s25, s25, 0
	global_load_lds_dwordx4 v[132:133], off
	s_mov_b32 m0, s81
	v_lshl_add_u64 v[132:133], s[24:25], 0, v[130:131]
	global_load_lds_dwordx4 v[132:133], off
	s_waitcnt vmcnt(8)
	s_waitcnt lgkmcnt(0)
	s_barrier
	s_setprio 1
	s_waitcnt lgkmcnt(0)
	v_mfma_i32_16x16x64_i8 v[60:63], v[136:139], v[174:177], v[60:63]
	v_mfma_i32_16x16x64_i8 v[52:55], v[146:149], v[174:177], v[52:55]
	v_mfma_i32_16x16x64_i8 v[44:47], v[136:139], v[182:185], v[44:47]
	v_mfma_i32_16x16x64_i8 v[36:39], v[146:149], v[182:185], v[36:39]
	v_mfma_i32_16x16x64_i8 v[28:31], v[136:139], v[190:193], v[28:31]
	v_mfma_i32_16x16x64_i8 v[20:23], v[146:149], v[190:193], v[20:23]
	v_mfma_i32_16x16x64_i8 v[12:15], v[136:139], v[198:201], v[12:15]
	v_mfma_i32_16x16x64_i8 v[4:7], v[146:149], v[198:201], v[4:7]
	v_mfma_i32_16x16x64_i8 v[60:63], v[140:143], v[178:181], v[60:63]
	v_mfma_i32_16x16x64_i8 v[52:55], v[150:153], v[178:181], v[52:55]
	v_mfma_i32_16x16x64_i8 v[44:47], v[140:143], v[186:189], v[44:47]
	v_mfma_i32_16x16x64_i8 v[36:39], v[150:153], v[186:189], v[36:39]
	v_mfma_i32_16x16x64_i8 v[28:31], v[140:143], v[194:197], v[28:31]
	v_mfma_i32_16x16x64_i8 v[20:23], v[150:153], v[194:197], v[20:23]
	v_mfma_i32_16x16x64_i8 v[12:15], v[140:143], v[202:205], v[12:15]
	v_mfma_i32_16x16x64_i8 v[4:7], v[150:153], v[202:205], v[4:7]
	s_setprio 0
	s_setprio 1
	v_mfma_i32_16x16x64_i8 v[56:59], v[154:157], v[174:177], v[56:59]
	v_mfma_i32_16x16x64_i8 v[48:51], v[166:169], v[174:177], v[48:51]
	v_mfma_i32_16x16x64_i8 v[40:43], v[154:157], v[182:185], v[40:43]
	v_mfma_i32_16x16x64_i8 v[32:35], v[166:169], v[182:185], v[32:35]
	v_mfma_i32_16x16x64_i8 v[24:27], v[154:157], v[190:193], v[24:27]
	v_mfma_i32_16x16x64_i8 v[16:19], v[166:169], v[190:193], v[16:19]
	v_mfma_i32_16x16x64_i8 v[8:11], v[154:157], v[198:201], v[8:11]
	v_mfma_i32_16x16x64_i8 v[0:3], v[166:169], v[198:201], v[0:3]
	v_mfma_i32_16x16x64_i8 v[56:59], v[158:161], v[178:181], v[56:59]
	v_mfma_i32_16x16x64_i8 v[48:51], v[170:173], v[178:181], v[48:51]
	v_mfma_i32_16x16x64_i8 v[40:43], v[158:161], v[186:189], v[40:43]
	v_mfma_i32_16x16x64_i8 v[32:35], v[170:173], v[186:189], v[32:35]
	v_mfma_i32_16x16x64_i8 v[24:27], v[158:161], v[194:197], v[24:27]
	v_mfma_i32_16x16x64_i8 v[16:19], v[170:173], v[194:197], v[16:19]
	v_mfma_i32_16x16x64_i8 v[8:11], v[158:161], v[202:205], v[8:11]
	v_mfma_i32_16x16x64_i8 v[0:3], v[170:173], v[202:205], v[0:3]
	s_setprio 0
	s_barrier
	s_add_i32 s19, s19, 2
	s_add_u32 s11, s11, 0x100
	s_addc_u32 s13, s13, 0
	s_add_u32 s22, s22, 0x100
	s_addc_u32 s23, s23, 0
	s_cmp_gt_u32 s19, 5
	s_cbranch_scc0 .LBB0_1540
	s_and_b64 vcc, exec, s[8:9]
	s_cbranch_vccz .LBB0_1543
	s_barrier

; template <bool I8, class AccT> __device__ __forceinline__ void mma1(AccT& c, const bf16x8& a, const bf16x8& b) {
;     if constexpr (I8) c = __builtin_amdgcn_mfma_i32_16x16x64_i8(__builtin_bit_cast(AccT, a), __builtin_bit_cast(AccT, b), c, 0, 0, 0);
;     else c = __builtin_amdgcn_mfma_f32_16x16x32_bf16(a, b, c, 0, 0, 0);
; }
.Lzdu_s0:
	v_mfma_i32_16x16x64_i8 v[126:129], v[132:135], v[174:177], 0
	v_mfma_i32_16x16x64_i8 v[118:121], v[142:145], v[174:177], 0
	v_mfma_i32_16x16x64_i8 v[108:111], v[132:135], v[182:185], 0
	v_mfma_i32_16x16x64_i8 v[100:103], v[142:145], v[182:185], 0
	v_mfma_i32_16x16x64_i8 v[92:95], v[132:135], v[190:193], 0
	v_mfma_i32_16x16x64_i8 v[84:87], v[142:145], v[190:193], 0
	v_mfma_i32_16x16x64_i8 v[76:79], v[132:135], v[198:201], 0
	v_mfma_i32_16x16x64_i8 v[68:71], v[142:145], v[198:201], 0
	v_mfma_i32_16x16x64_i8 v[126:129], v[138:141], v[178:181], v[126:129]
	v_mfma_i32_16x16x64_i8 v[118:121], v[150:153], v[178:181], v[118:121]
	v_mfma_i32_16x16x64_i8 v[108:111], v[138:141], v[186:189], v[108:111]
	v_mfma_i32_16x16x64_i8 v[100:103], v[150:153], v[186:189], v[100:103]
	v_mfma_i32_16x16x64_i8 v[92:95], v[138:141], v[194:197], v[92:95]
	v_mfma_i32_16x16x64_i8 v[84:87], v[150:153], v[194:197], v[84:87]
	v_mfma_i32_16x16x64_i8 v[76:79], v[138:141], v[202:205], v[76:79]
	v_mfma_i32_16x16x64_i8 v[68:71], v[150:153], v[202:205], v[68:71]
	s_setprio 0
	s_setprio 1
	v_mfma_i32_16x16x64_i8 v[122:125], v[154:157], v[174:177], 0
	v_mfma_i32_16x16x64_i8 v[114:117], v[166:169], v[174:177], 0
	v_mfma_i32_16x16x64_i8 v[104:107], v[154:157], v[182:185], 0
	v_mfma_i32_16x16x64_i8 v[96:99], v[166:169], v[182:185], 0
	v_mfma_i32_16x16x64_i8 v[88:91], v[154:157], v[190:193], 0
	v_mfma_i32_16x16x64_i8 v[80:83], v[166:169], v[190:193], 0
	v_mfma_i32_16x16x64_i8 v[72:75], v[154:157], v[198:201], 0
	v_mfma_i32_16x16x64_i8 v[64:67], v[166:169], v[198:201], 0
	v_mfma_i32_16x16x64_i8 v[122:125], v[158:161], v[178:181], v[122:125]
	v_mfma_i32_16x16x64_i8 v[114:117], v[170:173], v[178:181], v[114:117]
	v_mfma_i32_16x16x64_i8 v[104:107], v[158:161], v[186:189], v[104:107]
	v_mfma_i32_16x16x64_i8 v[96:99], v[170:173], v[186:189], v[96:99]
	v_mfma_i32_16x16x64_i8 v[88:91], v[158:161], v[194:197], v[88:91]
	v_mfma_i32_16x16x64_i8 v[80:83], v[170:173], v[194:197], v[80:83]
	v_mfma_i32_16x16x64_i8 v[72:75], v[158:161], v[202:205], v[72:75]
	v_mfma_i32_16x16x64_i8 v[64:67], v[170:173], v[202:205], v[64:67]
	s_setprio 0
	s_branch .Lzdu_r0
.Lzdu_s1:
	v_mfma_i32_16x16x64_i8 v[60:63], v[132:135], v[174:177], 0
	v_mfma_i32_16x16x64_i8 v[52:55], v[142:145], v[174:177], 0
	v_mfma_i32_16x16x64_i8 v[44:47], v[132:135], v[182:185], 0
	v_mfma_i32_16x16x64_i8 v[36:39], v[142:145], v[182:185], 0
	v_mfma_i32_16x16x64_i8 v[28:31], v[132:135], v[190:193], 0
	v_mfma_i32_16x16x64_i8 v[20:23], v[142:145], v[190:193], 0
	v_mfma_i32_16x16x64_i8 v[12:15], v[132:135], v[198:201], 0
	v_mfma_i32_16x16x64_i8 v[4:7], v[142:145], v[198:201], 0
	v_mfma_i32_16x16x64_i8 v[60:63], v[138:141], v[178:181], v[60:63]
	v_mfma_i32_16x16x64_i8 v[52:55], v[150:153], v[178:181], v[52:55]
	v_mfma_i32_16x16x64_i8 v[44:47], v[138:141], v[186:189], v[44:47]
	v_mfma_i32_16x16x64_i8 v[36:39], v[150:153], v[186:189], v[36:39]
	v_mfma_i32_16x16x64_i8 v[28:31], v[138:141], v[194:197], v[28:31]
	v_mfma_i32_16x16x64_i8 v[20:23], v[150:153], v[194:197], v[20:23]
	v_mfma_i32_16x16x64_i8 v[12:15], v[138:141], v[202:205], v[12:15]
	v_mfma_i32_16x16x64_i8 v[4:7], v[150:153], v[202:205], v[4:7]
	s_setprio 0
	s_setprio 1
	v_mfma_i32_16x16x64_i8 v[56:59], v[154:157], v[174:177], 0
	v_mfma_i32_16x16x64_i8 v[48:51], v[166:169], v[174:177], 0
	v_mfma_i32_16x16x64_i8 v[40:43], v[154:157], v[182:185], 0
	v_mfma_i32_16x16x64_i8 v[32:35], v[166:169], v[182:185], 0
	v_mfma_i32_16x16x64_i8 v[24:27], v[154:157], v[190:193], 0
	v_mfma_i32_16x16x64_i8 v[16:19], v[166:169], v[190:193], 0
	v_mfma_i32_16x16x64_i8 v[8:11], v[154:157], v[198:201], 0
	v_mfma_i32_16x16x64_i8 v[0:3], v[166:169], v[198:201], 0
	v_mfma_i32_16x16x64_i8 v[56:59], v[158:161], v[178:181], v[56:59]
	v_mfma_i32_16x16x64_i8 v[48:51], v[170:173], v[178:181], v[48:51]
	v_mfma_i32_16x16x64_i8 v[40:43], v[158:161], v[186:189], v[40:43]
	v_mfma_i32_16x16x64_i8 v[32:35], v[170:173], v[186:189], v[32:35]
	v_mfma_i32_16x16x64_i8 v[24:27], v[158:161], v[194:197], v[24:27]
	v_mfma_i32_16x16x64_i8 v[16:19], v[170:173], v[194:197], v[16:19]
	v_mfma_i32_16x16x64_i8 v[8:11], v[158:161], v[202:205], v[8:11]
	v_mfma_i32_16x16x64_i8 v[0:3], v[170:173], v[202:205], v[0:3]
	s_setprio 0
	s_branch .Lzdu_r1

; #define PG8_STAGE(bufoff, gbase, voff) do { _Pragma("unroll") for (int _i = 0; _i < 2; ++_i) { const char* gb_ = (const char*)(gbase) + _i * rstep; asm volatile("" : "+s"(gb_));   \
;         __builtin_amdgcn_global_load_lds((const unsigned*)(gb_ + (voff)), (LAS unsigned*)(lds + (bufoff) + ldsw + _i * 8192), 16, 0, 0); } } while (0)
; #define PG8_LDA(dst, b, h) do { _Pragma("unroll") for (int m = 0; m < 4; ++m) _Pragma("unroll") for (int k = 0; k < 2; ++k) dst[m][k] = *(const LAS bf16x8*)(lds + PG8_SA(b, h) + aoff + m * 2048 + k * 1024); } while (0)
; #define PG8_WAIT_V(n) asm volatile("s_waitcnt vmcnt(" #n ")" ::: "memory")
; #define PG8_WAIT_L(n) asm volatile("s_waitcnt lgkmcnt(" #n ")" ::: "memory")
; #define PG8_BAR __builtin_amdgcn_s_barrier()
; template <class Epi, class Sched, bool ALIGN_EPI = true, bool SP2 = true, bool I8 = false, bool F8 = false>
; __device__ __forceinline__ void gemm_phase(LAS unsigned char* lds, const int K, const Sched& S, const Epi& E, const int wave) {
;     ...
;         const bool has_next = S.next(ui + 1, nxt);
;         const char* nA = has_next ? nxt.a : cA; const char* nB = has_next ? nxt.b : cB;
;         for (int t = 0; t < nt; t += 2) {
;             const bool last = (t == nt - 2);
;             const char* a1 = cA + (size_t)(t + 1) * kstep;
;             const char* a2 = last ? nA : cA + (size_t)(t + 2) * kstep; const char* b2 = last ? nB : cB + (size_t)(t + 2) * kstep;
;             const char* a3 = a2 + kstep; const char* b3 = b2 + kstep;
;             if constexpr (SP2) {
;             PG8_LDB(B0, 0, 0); PG8_LDB(B1, 0, 1); PG8_SCHED; PG8_LDA(At, 0, 0); PG8_STAGE(PG8_SA(1, 1), a1 + hstep, voffA);
;             PG8_WAIT_V(8); PG8_WAIT_L(0); PG8_BAR; PG8_MMA(0, 0, At, B0); PG8_MMA(0, 1, At, B1); PG8_BAR; PG8_SCHED;
;             PG8_LDA(At, 0, 1); PG8_STAGE(PG8_SB(0, 0), b2, voffB); PG8_STAGE(PG8_SB(0, 1), b2 + hstep, voffB); PG8_STAGE(PG8_SA(0, 0), a2, voffA);
;             PG8_WAIT_V(8); PG8_WAIT_L(0); PG8_BAR; PG8_MMA(1, 0, At, B0); PG8_MMA(1, 1, At, B1); PG8_BAR; PG8_SCHED;
;     ...
;         if (!(Epi::KEEPS && cur.sub < 2)) {
; #pragma unroll
;         for (int a = 0; a < 2; ++a)
; #pragma unroll
;             for (int b = 0; b < 2; ++b)
; #pragma unroll
;                 for (int m = 0; m < 4; ++m)
; #pragma unroll
;                     for (int n = 0; n < 2; ++n) acc[a][b][m][n] = (acc_t){0, 0, 0, 0};
;         }
.LBB0_1766:
	s_add_u32 s9, s20, 0x100
	s_addc_u32 s11, s21, 0
	s_add_u32 s18, s18, 0x30080
	s_addc_u32 s19, s19, 0
	s_mov_b32 s46, -2
.LBB0_1767:
	s_add_u32 s20, s18, 0xfffd0080
	s_addc_u32 s21, s19, -1
	s_cmp_eq_u32 s46, 4
	s_cselect_b32 s20, s12, s20
	s_cselect_b32 s21, s13, s21
	s_cselect_b32 s24, s14, s9
	s_cselect_b32 s25, s15, s11
	s_add_u32 s22, s20, 0x80
	s_addc_u32 s23, s21, 0
	s_add_i32 s47, 0, 0x10000
	v_add_u32_e32 v136, s47, v137
	s_add_i32 s50, 0, 0x14000
	ds_read_b128 v[132:135], v136
	ds_read_b128 v[138:141], v136 offset:1024
	ds_read_b128 v[142:145], v136 offset:2048
	ds_read_b128 v[150:153], v136 offset:3072
	v_add_u32_e32 v136, s50, v137
	ds_read_b128 v[154:157], v136
	ds_read_b128 v[158:161], v136 offset:1024
	ds_read_b128 v[166:169], v136 offset:2048
	ds_read_b128 v[170:173], v136 offset:3072
	s_add_u32 s48, s18, 0xffff0000
	s_addc_u32 s49, s19, -1
	ds_read_b128 v[174:177], v149
	ds_read_b128 v[178:181], v149 offset:1024
	ds_read_b128 v[182:185], v149 offset:2048
	ds_read_b128 v[186:189], v149 offset:3072
	ds_read_b128 v[190:193], v149 offset:4096
	ds_read_b128 v[194:197], v149 offset:5120
	ds_read_b128 v[198:201], v149 offset:6144
	ds_read_b128 v[202:205], v149 offset:7168
	s_add_i32 m0, s38, 0xc000
	v_lshl_add_u64 v[146:147], s[48:49], 0, v[130:131]
	s_mov_b64 s[48:49], s[18:19]
	global_load_lds_dwordx4 v[146:147], off
	s_add_i32 m0, s38, 0xe000
	v_lshl_add_u64 v[146:147], s[48:49], 0, v[130:131]
	global_load_lds_dwordx4 v[146:147], off
	s_waitcnt vmcnt(8)
	s_waitcnt lgkmcnt(0)
	s_barrier
	s_setprio 1
	s_waitcnt lgkmcnt(0)
	s_cmp_eq_u32 s46, -2
	s_cbranch_scc1 .Lzdu_s0
	v_mfma_i32_16x16x64_i8 v[126:129], v[132:135], v[174:177], v[126:129]
	v_mfma_i32_16x16x64_i8 v[118:121], v[142:145], v[174:177], v[118:121]
	v_mfma_i32_16x16x64_i8 v[108:111], v[132:135], v[182:185], v[108:111]
	v_mfma_i32_16x16x64_i8 v[100:103], v[142:145], v[182:185], v[100:103]
	v_mfma_i32_16x16x64_i8 v[92:95], v[132:135], v[190:193], v[92:95]
	v_mfma_i32_16x16x64_i8 v[84:87], v[142:145], v[190:193], v[84:87]
	v_mfma_i32_16x16x64_i8 v[76:79], v[132:135], v[198:201], v[76:79]
	v_mfma_i32_16x16x64_i8 v[68:71], v[142:145], v[198:201], v[68:71]
	v_mfma_i32_16x16x64_i8 v[126:129], v[138:141], v[178:181], v[126:129]
	v_mfma_i32_16x16x64_i8 v[118:121], v[150:153], v[178:181], v[118:121]
	v_mfma_i32_16x16x64_i8 v[108:111], v[138:141], v[186:189], v[108:111]
	v_mfma_i32_16x16x64_i8 v[100:103], v[150:153], v[186:189], v[100:103]
	v_mfma_i32_16x16x64_i8 v[92:95], v[138:141], v[194:197], v[92:95]
	v_mfma_i32_16x16x64_i8 v[84:87], v[150:153], v[194:197], v[84:87]
	v_mfma_i32_16x16x64_i8 v[76:79], v[138:141], v[202:205], v[76:79]
	v_mfma_i32_16x16x64_i8 v[68:71], v[150:153], v[202:205], v[68:71]
	s_setprio 0
	s_setprio 1
	v_mfma_i32_16x16x64_i8 v[122:125], v[154:157], v[174:177], v[122:125]
	v_mfma_i32_16x16x64_i8 v[114:117], v[166:169], v[174:177], v[114:117]
	v_mfma_i32_16x16x64_i8 v[104:107], v[154:157], v[182:185], v[104:107]
	v_mfma_i32_16x16x64_i8 v[96:99], v[166:169], v[182:185], v[96:99]
	v_mfma_i32_16x16x64_i8 v[88:91], v[154:157], v[190:193], v[88:91]
	v_mfma_i32_16x16x64_i8 v[80:83], v[166:169], v[190:193], v[80:83]
	v_mfma_i32_16x16x64_i8 v[72:75], v[154:157], v[198:201], v[72:75]
	v_mfma_i32_16x16x64_i8 v[64:67], v[166:169], v[198:201], v[64:67]
	v_mfma_i32_16x16x64_i8 v[122:125], v[158:161], v[178:181], v[122:125]
	v_mfma_i32_16x16x64_i8 v[114:117], v[170:173], v[178:181], v[114:117]
	v_mfma_i32_16x16x64_i8 v[104:107], v[158:161], v[186:189], v[104:107]
	v_mfma_i32_16x16x64_i8 v[96:99], v[170:173], v[186:189], v[96:99]
	v_mfma_i32_16x16x64_i8 v[88:91], v[158:161], v[194:197], v[88:91]
	v_mfma_i32_16x16x64_i8 v[80:83], v[170:173], v[194:197], v[80:83]
	v_mfma_i32_16x16x64_i8 v[72:75], v[158:161], v[202:205], v[72:75]
	v_mfma_i32_16x16x64_i8 v[64:67], v[170:173], v[202:205], v[64:67]
	s_setprio 0
.Lzdu_r0:
	s_barrier
	s_mov_b64 s[48:49], s[24:25]
	ds_read_b128 v[174:177], v149 offset:16384
	ds_read_b128 v[178:181], v149 offset:17408
	ds_read_b128 v[182:185], v149 offset:18432
	ds_read_b128 v[186:189], v149 offset:19456
	ds_read_b128 v[190:193], v149 offset:20480
	ds_read_b128 v[194:197], v149 offset:21504
	ds_read_b128 v[198:201], v149 offset:22528
	ds_read_b128 v[202:205], v149 offset:23552
	s_add_i32 s47, s47, s28
	v_lshl_add_u64 v[146:147], s[48:49], 0, v[112:113]
	s_add_u32 s48, s24, 0x10000
	s_mov_b32 m0, s47
	s_addc_u32 s49, s25, 0
	global_load_lds_dwordx4 v[146:147], off
	s_add_i32 m0, s47, 0x2000
	v_lshl_add_u64 v[146:147], s[48:49], 0, v[112:113]
	s_add_u32 s48, s24, 0x20000
	s_addc_u32 s49, s25, 0
	global_load_lds_dwordx4 v[146:147], off
	s_add_i32 s47, s50, s28
	v_lshl_add_u64 v[146:147], s[48:49], 0, v[112:113]
	s_add_u32 s48, s24, 0x30000
	s_mov_b32 m0, s47
	s_addc_u32 s49, s25, 0
	global_load_lds_dwordx4 v[146:147], off
	s_add_i32 m0, s47, 0x2000
	v_lshl_add_u64 v[146:147], s[48:49], 0, v[112:113]
	s_mov_b64 s[48:49], s[20:21]
	global_load_lds_dwordx4 v[146:147], off
	s_mov_b32 m0, s38
	v_lshl_add_u64 v[146:147], s[48:49], 0, v[130:131]
	s_add_u32 s48, s20, 0x10000
	s_addc_u32 s49, s21, 0
	global_load_lds_dwordx4 v[146:147], off
	s_mov_b32 m0, s39
	v_lshl_add_u64 v[146:147], s[48:49], 0, v[130:131]
	global_load_lds_dwordx4 v[146:147], off
	s_waitcnt vmcnt(8)
	s_waitcnt lgkmcnt(0)
	s_barrier
	s_setprio 1
	s_waitcnt lgkmcnt(0)
	s_cmp_eq_u32 s46, -2
	s_cbranch_scc1 .Lzdu_s1
; #define PG8_STAGE(bufoff, gbase, voff) do { _Pragma("unroll") for (int _i = 0; _i < 2; ++_i) { const char* gb_ = (const char*)(gbase) + _i * rstep; asm volatile("" : "+s"(gb_));   \
;         __builtin_amdgcn_global_load_lds((const unsigned*)(gb_ + (voff)), (LAS unsigned*)(lds + (bufoff) + ldsw + _i * 8192), 16, 0, 0); } } while (0)
; #define PG8_LDA(dst, b, h) do { _Pragma("unroll") for (int m = 0; m < 4; ++m) _Pragma("unroll") for (int k = 0; k < 2; ++k) dst[m][k] = *(const LAS bf16x8*)(lds + PG8_SA(b, h) + aoff + m * 2048 + k * 1024); } while (0)
; #define PG8_LDB(dst, b, h) do { _Pragma("unroll") for (int n = 0; n < 2; ++n) _Pragma("unroll") for (int k = 0; k < 2; ++k) dst[n][k] = *(const LAS bf16x8*)(lds + PG8_SB(b, h) + boff + n * 2048 + k * 1024); } while (0)
; #define PG8_WAIT_V(n) asm volatile("s_waitcnt vmcnt(" #n ")" ::: "memory")
; #define PG8_WAIT_L(n) asm volatile("s_waitcnt lgkmcnt(" #n ")" ::: "memory")
; #define PG8_BAR __builtin_amdgcn_s_barrier()
; #define PG8_SCHED __builtin_amdgcn_sched_barrier(0)
; template <class Epi, class Sched, bool ALIGN_EPI = true, bool SP2 = true, bool I8 = false, bool F8 = false>
; __device__ __forceinline__ void gemm_phase(LAS unsigned char* lds, const int K, const Sched& S, const Epi& E, const int wave) {
;     ...
;             PG8_WAIT_V(8); PG8_WAIT_L(0); PG8_BAR; PG8_MMA(1, 0, At, B0); PG8_MMA(1, 1, At, B1); PG8_BAR; PG8_SCHED;
;             PG8_LDB(B0, 1, 0); PG8_LDB(B1, 1, 1); PG8_SCHED; PG8_LDA(At, 1, 0); PG8_STAGE(PG8_SA(0, 1), a2 + hstep, voffA);
;             PG8_WAIT_V(8); PG8_WAIT_L(0); PG8_BAR; PG8_MMA(0, 0, At, B0); PG8_MMA(0, 1, At, B1); PG8_BAR; PG8_SCHED;
	v_mfma_i32_16x16x64_i8 v[60:63], v[132:135], v[174:177], v[60:63]
	v_mfma_i32_16x16x64_i8 v[52:55], v[142:145], v[174:177], v[52:55]
	v_mfma_i32_16x16x64_i8 v[44:47], v[132:135], v[182:185], v[44:47]
	v_mfma_i32_16x16x64_i8 v[36:39], v[142:145], v[182:185], v[36:39]
	v_mfma_i32_16x16x64_i8 v[28:31], v[132:135], v[190:193], v[28:31]
	v_mfma_i32_16x16x64_i8 v[20:23], v[142:145], v[190:193], v[20:23]
	v_mfma_i32_16x16x64_i8 v[12:15], v[132:135], v[198:201], v[12:15]
	v_mfma_i32_16x16x64_i8 v[4:7], v[142:145], v[198:201], v[4:7]
	v_mfma_i32_16x16x64_i8 v[60:63], v[138:141], v[178:181], v[60:63]
	v_mfma_i32_16x16x64_i8 v[52:55], v[150:153], v[178:181], v[52:55]
	v_mfma_i32_16x16x64_i8 v[44:47], v[138:141], v[186:189], v[44:47]
	v_mfma_i32_16x16x64_i8 v[36:39], v[150:153], v[186:189], v[36:39]
	v_mfma_i32_16x16x64_i8 v[28:31], v[138:141], v[194:197], v[28:31]
	v_mfma_i32_16x16x64_i8 v[20:23], v[150:153], v[194:197], v[20:23]
	v_mfma_i32_16x16x64_i8 v[12:15], v[138:141], v[202:205], v[12:15]
	v_mfma_i32_16x16x64_i8 v[4:7], v[150:153], v[202:205], v[4:7]
	s_setprio 0
	s_setprio 1
	v_mfma_i32_16x16x64_i8 v[56:59], v[154:157], v[174:177], v[56:59]
	v_mfma_i32_16x16x64_i8 v[48:51], v[166:169], v[174:177], v[48:51]
	v_mfma_i32_16x16x64_i8 v[40:43], v[154:157], v[182:185], v[40:43]
	v_mfma_i32_16x16x64_i8 v[32:35], v[166:169], v[182:185], v[32:35]
	v_mfma_i32_16x16x64_i8 v[24:27], v[154:157], v[190:193], v[24:27]
	v_mfma_i32_16x16x64_i8 v[16:19], v[166:169], v[190:193], v[16:19]
	v_mfma_i32_16x16x64_i8 v[8:11], v[154:157], v[198:201], v[8:11]
	v_mfma_i32_16x16x64_i8 v[0:3], v[166:169], v[198:201], v[0:3]
	v_mfma_i32_16x16x64_i8 v[56:59], v[158:161], v[178:181], v[56:59]
	v_mfma_i32_16x16x64_i8 v[48:51], v[170:173], v[178:181], v[48:51]
	v_mfma_i32_16x16x64_i8 v[40:43], v[158:161], v[186:189], v[40:43]
	v_mfma_i32_16x16x64_i8 v[32:35], v[170:173], v[186:189], v[32:35]
	v_mfma_i32_16x16x64_i8 v[24:27], v[158:161], v[194:197], v[24:27]
	v_mfma_i32_16x16x64_i8 v[16:19], v[170:173], v[194:197], v[16:19]
	v_mfma_i32_16x16x64_i8 v[8:11], v[158:161], v[202:205], v[8:11]
	v_mfma_i32_16x16x64_i8 v[0:3], v[170:173], v[202:205], v[0:3]
	s_setprio 0
.Lzdu_r1:
	s_barrier
	s_add_i32 s47, 0, 0x18000
	v_add_u32_e32 v136, s47, v137
	s_add_i32 s50, 0, 0x1c000
	ds_read_b128 v[132:135], v136
	ds_read_b128 v[138:141], v136 offset:1024
	ds_read_b128 v[142:145], v136 offset:2048
	ds_read_b128 v[150:153], v136 offset:3072
	v_add_u32_e32 v136, s50, v137
	ds_read_b128 v[154:157], v136
	ds_read_b128 v[158:161], v136 offset:1024
	ds_read_b128 v[166:169], v136 offset:2048
	ds_read_b128 v[170:173], v136 offset:3072
	s_add_u32 s48, s20, 0x20000
	s_addc_u32 s49, s21, 0
	ds_read_b128 v[174:177], v149 offset:32768
	ds_read_b128 v[178:181], v149 offset:33792
	ds_read_b128 v[182:185], v149 offset:34816
	ds_read_b128 v[186:189], v149 offset:35840
	ds_read_b128 v[190:193], v149 offset:36864
	ds_read_b128 v[194:197], v149 offset:37888
	ds_read_b128 v[198:201], v149 offset:38912
	ds_read_b128 v[202:205], v149 offset:39936
	s_mov_b32 m0, s40
	v_lshl_add_u64 v[146:147], s[48:49], 0, v[130:131]
	s_add_u32 s48, s20, 0x30000
	s_addc_u32 s49, s21, 0
	global_load_lds_dwordx4 v[146:147], off
	s_mov_b32 m0, s41
	v_lshl_add_u64 v[146:147], s[48:49], 0, v[130:131]
	global_load_lds_dwordx4 v[146:147], off
	s_waitcnt vmcnt(8)
	s_waitcnt lgkmcnt(0)
	s_barrier
	s_setprio 1
	s_waitcnt lgkmcnt(0)
	v_mfma_i32_16x16x64_i8 v[126:129], v[132:135], v[174:177], v[126:129]
	v_mfma_i32_16x16x64_i8 v[118:121], v[142:145], v[174:177], v[118:121]
	v_mfma_i32_16x16x64_i8 v[108:111], v[132:135], v[182:185], v[108:111]
	v_mfma_i32_16x16x64_i8 v[100:103], v[142:145], v[182:185], v[100:103]
	v_mfma_i32_16x16x64_i8 v[92:95], v[132:135], v[190:193], v[92:95]
	v_mfma_i32_16x16x64_i8 v[84:87], v[142:145], v[190:193], v[84:87]
	v_mfma_i32_16x16x64_i8 v[76:79], v[132:135], v[198:201], v[76:79]
	v_mfma_i32_16x16x64_i8 v[68:71], v[142:145], v[198:201], v[68:71]
	v_mfma_i32_16x16x64_i8 v[126:129], v[138:141], v[178:181], v[126:129]
	v_mfma_i32_16x16x64_i8 v[118:121], v[150:153], v[178:181], v[118:121]
	v_mfma_i32_16x16x64_i8 v[108:111], v[138:141], v[186:189], v[108:111]
	v_mfma_i32_16x16x64_i8 v[100:103], v[150:153], v[186:189], v[100:103]
	v_mfma_i32_16x16x64_i8 v[92:95], v[138:141], v[194:197], v[92:95]
	v_mfma_i32_16x16x64_i8 v[84:87], v[150:153], v[194:197], v[84:87]
	v_mfma_i32_16x16x64_i8 v[76:79], v[138:141], v[202:205], v[76:79]
	v_mfma_i32_16x16x64_i8 v[68:71], v[150:153], v[202:205], v[68:71]
	s_setprio 0
	s_setprio 1
	v_mfma_i32_16x16x64_i8 v[122:125], v[154:157], v[174:177], v[122:125]
	v_mfma_i32_16x16x64_i8 v[114:117], v[166:169], v[174:177], v[114:117]
	v_mfma_i32_16x16x64_i8 v[104:107], v[154:157], v[182:185], v[104:107]
	v_mfma_i32_16x16x64_i8 v[96:99], v[166:169], v[182:185], v[96:99]
	v_mfma_i32_16x16x64_i8 v[88:91], v[154:157], v[190:193], v[88:91]
	v_mfma_i32_16x16x64_i8 v[80:83], v[166:169], v[190:193], v[80:83]
	v_mfma_i32_16x16x64_i8 v[72:75], v[154:157], v[198:201], v[72:75]
	v_mfma_i32_16x16x64_i8 v[64:67], v[166:169], v[198:201], v[64:67]
	v_mfma_i32_16x16x64_i8 v[122:125], v[158:161], v[178:181], v[122:125]
	v_mfma_i32_16x16x64_i8 v[114:117], v[170:173], v[178:181], v[114:117]
	v_mfma_i32_16x16x64_i8 v[104:107], v[158:161], v[186:189], v[104:107]
	v_mfma_i32_16x16x64_i8 v[96:99], v[170:173], v[186:189], v[96:99]
	v_mfma_i32_16x16x64_i8 v[88:91], v[158:161], v[194:197], v[88:91]
	v_mfma_i32_16x16x64_i8 v[80:83], v[170:173], v[194:197], v[80:83]
	v_mfma_i32_16x16x64_i8 v[72:75], v[158:161], v[202:205], v[72:75]
	v_mfma_i32_16x16x64_i8 v[64:67], v[170:173], v[202:205], v[64:67]
	s_setprio 0
	s_barrier
; #define PG8_STAGE(bufoff, gbase, voff) do { _Pragma("unroll") for (int _i = 0; _i < 2; ++_i) { const char* gb_ = (const char*)(gbase) + _i * rstep; asm volatile("" : "+s"(gb_));   \
;         __builtin_amdgcn_global_load_lds((const unsigned*)(gb_ + (voff)), (LAS unsigned*)(lds + (bufoff) + ldsw + _i * 8192), 16, 0, 0); } } while (0)
; #define PG8_LDA(dst, b, h) do { _Pragma("unroll") for (int m = 0; m < 4; ++m) _Pragma("unroll") for (int k = 0; k < 2; ++k) dst[m][k] = *(const LAS bf16x8*)(lds + PG8_SA(b, h) + aoff + m * 2048 + k * 1024); } while (0)
; #define PG8_WAIT_V(n) asm volatile("s_waitcnt vmcnt(" #n ")" ::: "memory")
; #define PG8_WAIT_L(n) asm volatile("s_waitcnt lgkmcnt(" #n ")" ::: "memory")
; #define PG8_BAR __builtin_amdgcn_s_barrier()
; #define PG8_SCHED __builtin_amdgcn_sched_barrier(0)
; template <class Epi, class Sched, bool ALIGN_EPI = true, bool SP2 = true, bool I8 = false, bool F8 = false>
; __device__ __forceinline__ void gemm_phase(LAS unsigned char* lds, const int K, const Sched& S, const Epi& E, const int wave) {
;     ...
;         for (int t = 0; t < nt; t += 2) {
;             const bool last = (t == nt - 2);
;     ...
;             PG8_LDA(At, 1, 1); PG8_STAGE(PG8_SB(1, 0), b3, voffB); PG8_STAGE(PG8_SB(1, 1), b3 + hstep, voffB); PG8_STAGE(PG8_SA(1, 0), a3, voffA);
;             PG8_WAIT_V(8); PG8_WAIT_L(0); PG8_BAR; PG8_MMA(1, 0, At, B0); PG8_MMA(1, 1, At, B1); PG8_BAR; PG8_SCHED;
	s_add_u32 s48, s24, 0x80
	s_addc_u32 s49, s25, 0
	ds_read_b128 v[174:177], v149 offset:49152
	ds_read_b128 v[178:181], v149 offset:50176
	ds_read_b128 v[182:185], v149 offset:51200
	ds_read_b128 v[186:189], v149 offset:52224
	ds_read_b128 v[190:193], v149 offset:53248
	ds_read_b128 v[194:197], v149 offset:54272
	ds_read_b128 v[198:201], v149 offset:55296
	ds_read_b128 v[202:205], v149 offset:56320
	s_add_i32 s47, s47, s28
	v_lshl_add_u64 v[146:147], s[48:49], 0, v[112:113]
	s_add_u32 s48, s24, 0x10080
	s_mov_b32 m0, s47
	s_addc_u32 s49, s25, 0
	global_load_lds_dwordx4 v[146:147], off
	s_add_i32 m0, s47, 0x2000
	v_lshl_add_u64 v[146:147], s[48:49], 0, v[112:113]
	s_add_u32 s48, s24, 0x20080
	s_addc_u32 s49, s25, 0
	s_add_i32 s47, s50, s28
	global_load_lds_dwordx4 v[146:147], off
	s_mov_b32 m0, s47
	v_lshl_add_u64 v[146:147], s[48:49], 0, v[112:113]
	s_add_u32 s24, s24, 0x30080
	global_load_lds_dwordx4 v[146:147], off
	s_addc_u32 s25, s25, 0
	s_add_i32 m0, s47, 0x2000
	s_add_u32 s20, s20, 0x10080
	v_lshl_add_u64 v[146:147], s[24:25], 0, v[112:113]
	global_load_lds_dwordx4 v[146:147], off
	s_mov_b32 m0, s43
	v_lshl_add_u64 v[146:147], s[22:23], 0, v[130:131]
	s_addc_u32 s21, s21, 0
	global_load_lds_dwordx4 v[146:147], off
	s_mov_b32 m0, s44
	v_lshl_add_u64 v[146:147], s[20:21], 0, v[130:131]
	global_load_lds_dwordx4 v[146:147], off
	s_waitcnt vmcnt(8)
	s_waitcnt lgkmcnt(0)
	s_barrier
	s_setprio 1
	s_waitcnt lgkmcnt(0)
	v_mfma_i32_16x16x64_i8 v[60:63], v[132:135], v[174:177], v[60:63]
	v_mfma_i32_16x16x64_i8 v[52:55], v[142:145], v[174:177], v[52:55]
	v_mfma_i32_16x16x64_i8 v[44:47], v[132:135], v[182:185], v[44:47]
	v_mfma_i32_16x16x64_i8 v[36:39], v[142:145], v[182:185], v[36:39]
	v_mfma_i32_16x16x64_i8 v[28:31], v[132:135], v[190:193], v[28:31]
	v_mfma_i32_16x16x64_i8 v[20:23], v[142:145], v[190:193], v[20:23]
	v_mfma_i32_16x16x64_i8 v[12:15], v[132:135], v[198:201], v[12:15]
	v_mfma_i32_16x16x64_i8 v[4:7], v[142:145], v[198:201], v[4:7]
	v_mfma_i32_16x16x64_i8 v[60:63], v[138:141], v[178:181], v[60:63]
	v_mfma_i32_16x16x64_i8 v[52:55], v[150:153], v[178:181], v[52:55]
	v_mfma_i32_16x16x64_i8 v[44:47], v[138:141], v[186:189], v[44:47]
	v_mfma_i32_16x16x64_i8 v[36:39], v[150:153], v[186:189], v[36:39]
	v_mfma_i32_16x16x64_i8 v[28:31], v[138:141], v[194:197], v[28:31]
	v_mfma_i32_16x16x64_i8 v[20:23], v[150:153], v[194:197], v[20:23]
	v_mfma_i32_16x16x64_i8 v[12:15], v[138:141], v[202:205], v[12:15]
	v_mfma_i32_16x16x64_i8 v[4:7], v[150:153], v[202:205], v[4:7]
	s_setprio 0
	s_setprio 1
	v_mfma_i32_16x16x64_i8 v[56:59], v[154:157], v[174:177], v[56:59]
	v_mfma_i32_16x16x64_i8 v[48:51], v[166:169], v[174:177], v[48:51]
	v_mfma_i32_16x16x64_i8 v[40:43], v[154:157], v[182:185], v[40:43]
	v_mfma_i32_16x16x64_i8 v[32:35], v[166:169], v[182:185], v[32:35]
	v_mfma_i32_16x16x64_i8 v[24:27], v[154:157], v[190:193], v[24:27]
	v_mfma_i32_16x16x64_i8 v[16:19], v[166:169], v[190:193], v[16:19]
	v_mfma_i32_16x16x64_i8 v[8:11], v[154:157], v[198:201], v[8:11]
	v_mfma_i32_16x16x64_i8 v[0:3], v[166:169], v[198:201], v[0:3]
	v_mfma_i32_16x16x64_i8 v[56:59], v[158:161], v[178:181], v[56:59]
	v_mfma_i32_16x16x64_i8 v[48:51], v[170:173], v[178:181], v[48:51]
	v_mfma_i32_16x16x64_i8 v[40:43], v[158:161], v[186:189], v[40:43]
	v_mfma_i32_16x16x64_i8 v[32:35], v[170:173], v[186:189], v[32:35]
	v_mfma_i32_16x16x64_i8 v[24:27], v[158:161], v[194:197], v[24:27]
	v_mfma_i32_16x16x64_i8 v[16:19], v[170:173], v[194:197], v[16:19]
	v_mfma_i32_16x16x64_i8 v[8:11], v[158:161], v[202:205], v[8:11]
	v_mfma_i32_16x16x64_i8 v[0:3], v[170:173], v[202:205], v[0:3]
	s_setprio 0
	s_barrier
	s_add_i32 s46, s46, 2
	s_add_u32 s9, s9, 0x100
	s_addc_u32 s11, s11, 0
	s_add_u32 s18, s18, 0x100
	s_addc_u32 s19, s19, 0
	s_cmp_gt_u32 s46, 5
	s_cbranch_scc0 .LBB0_1767
	s_and_b64 vcc, exec, s[4:5]
	s_cbranch_vccz .LBB0_1770
	s_barrier
